# P9 and P10 unit top: the three expert-indexed LDS table reads (ucum, segoff, cnt) issued together behind one wait
# baseline (speedup 1.0000x reference)
.LBB0_872:
	s_add_i32 s29, s6, 1
	s_cmpk_gt_u32 s6, 0xfe
	s_mov_b64 s[54:55], 0
	s_cbranch_scc1 .LBB0_875
	s_lshl_b32 s4, s29, 2
	s_add_i32 s4, s4, 0
	s_add_i32 s4, s4, 0x21160
	v_mov_b32_e32 v2, s4
	ds_read_b32 v2, v2
	s_waitcnt lgkmcnt(0)
	v_cmp_gt_i32_e32 vcc, 0, v2
	v_readfirstlane_b32 s4, v2
	s_cbranch_vccnz .LBB0_875
	s_lshl_b32 s1, s4, 2
	s_add_i32 s1, s1, 0
	s_add_i32 s7, s1, 0x20200
	v_mov_b32_e32 v3, s7
	ds_read_b32 v2, v3
	ds_read_b32 v4, v3 offset:288
	ds_read_b32 v5, v3 offset:576
	s_mul_i32 s0, s29, s33
	s_add_i32 s0, s0, s64
	s_mov_b32 s5, s48
	s_mov_b64 s[54:55], -1
	s_waitcnt lgkmcnt(0)
	v_readfirstlane_b32 s7, v2
	s_sub_i32 s0, s0, s7
	s_ashr_i32 s7, s0, 31
	s_lshr_b32 s7, s7, 30
	s_add_i32 s7, s0, s7
	s_ashr_i32 s28, s7, 2
	s_and_b32 s7, s7, -4
	s_sub_i32 s38, s0, s7
	s_lshl_b32 s0, s28, 8
	s_mov_b32 s96, s4
	v_add_u32_e32 v217, s0, v4
	s_lshl_b64 s[0:1], s[4:5], 21
	s_add_u32 s5, s10, s0
	s_addc_u32 s7, s11, s1
	s_ashr_i32 s39, s38, 31
	s_lshl_b64 s[0:1], s[38:39], 19
	s_add_u32 s0, s5, s0
	s_addc_u32 s1, s7, s1
.LBB0_875:
	s_and_b64 s[4:5], s[54:55], s[84:85]
	s_andn2_b64 vcc, exec, s[4:5]
	s_cbranch_vccnz .LBB0_877
	s_ashr_i32 s97, s96, 31
	v_lshl_add_u32 v3, s28, 8, v211
	s_lshl_b64 s[4:5], s[96:97], 17
	s_add_u32 s4, s93, s4
	v_add_u32_e32 v2, -1, v5
	v_min_i32_e32 v2, v3, v2
	s_addc_u32 s5, s14, s5
	v_ashrrev_i32_e32 v3, 31, v2
	v_lshl_add_u64 v[2:3], v[2:3], 2, s[4:5]
	s_lshl_b32 s4, s29, 10
	s_and_b32 s4, s4, 0x400
	s_add_i32 m0, s25, s4
	s_nop 0
	global_load_lds_dword v[2:3], off

.LBB0_978:
	s_add_i32 s30, s16, 1
	s_cmpk_gt_u32 s16, 0xfe
	s_mov_b64 s[92:93], 0
	s_cbranch_scc1 .LBB0_981
	s_lshl_b32 s4, s30, 2
	s_add_i32 s4, s4, 0
	s_add_i32 s4, s4, 0x21160
	v_mov_b32_e32 v2, s4
	ds_read_b32 v2, v2
	s_waitcnt lgkmcnt(0)
	v_cmp_gt_i32_e32 vcc, 0, v2
	v_readfirstlane_b32 s4, v2
	s_cbranch_vccnz .LBB0_981
	s_lshl_b32 s7, s4, 2
	s_add_i32 s7, s7, 0
	s_add_i32 s17, s7, 0x20200
	v_mov_b32_e32 v3, s17
	ds_read_b32 v2, v3
	ds_read_b32 v232, v3 offset:288
	ds_read_b32 v207, v3 offset:576
	s_mul_i32 s5, s30, s33
	s_add_i32 s6, s5, s64
	s_add_i32 s7, s7, 0x20320
	s_mov_b32 s5, s48
	s_waitcnt lgkmcnt(0)
	v_readfirstlane_b32 s17, v2
	s_sub_i32 s6, s6, s17
	s_ashr_i32 s17, s6, 31
	s_lshr_b32 s17, s17, 29
	s_add_i32 s17, s6, s17
	s_ashr_i32 s91, s17, 3
	s_and_b32 s17, s17, -8
	s_sub_i32 s6, s6, s17
	s_mul_i32 s17, s30, 0xab
	s_bfe_u32 s17, s17, 0x70009
	s_mul_i32 s17, s17, 3
	s_sub_i32 s17, s30, s17
	s_and_b32 s17, s17, 0xff
	s_lshl_b32 s17, s17, 8
	s_or_b32 s31, s6, s17
	s_lshl_b32 s7, s91, 8
	v_readfirstlane_b32 s17, v232
	s_add_i32 s38, s7, s17
	s_ashr_i32 s39, s38, 31
	s_lshl_b64 s[38:39], s[38:39], 9
	s_add_u32 s38, s2, s38
	s_addc_u32 s39, s3, s39
	s_lshl_b64 s[50:51], s[4:5], 20
	s_add_u32 s5, s8, s50
	s_addc_u32 s17, s9, s51
	s_ashr_i32 s7, s6, 31
	s_lshl_b64 s[6:7], s[6:7], 17
	s_add_u32 s84, s5, s6
	s_addc_u32 s85, s17, s7
	s_mov_b64 s[92:93], -1
	s_mov_b32 s86, s4
.LBB0_981:
	s_and_b64 s[4:5], s[36:37], s[92:93]
	s_andn2_b64 vcc, exec, s[4:5]
	s_cbranch_vccnz .LBB0_983
	s_ashr_i32 s87, s86, 31
	v_lshl_add_u32 v3, s91, 8, v200
	s_lshl_b64 s[4:5], s[86:87], 17
	s_add_u32 s4, s12, s4
	v_add_u32_e32 v2, -1, v207
	v_min_i32_e32 v2, v3, v2
	s_addc_u32 s5, s13, s5
	v_ashrrev_i32_e32 v3, 31, v2
	v_lshl_add_u64 v[2:3], v[2:3], 2, s[4:5]
	s_mul_hi_u32 s4, s30, 0xaaaaaaab
	s_lshr_b32 s4, s4, 1
	s_mul_i32 s4, s4, 3
	s_sub_i32 s4, s30, s4
	s_lshl_b32 s4, s4, 10
	s_add_i32 m0, s29, s4
	s_nop 0
	global_load_lds_dword v[2:3], off
